# A-phase tail: idle CUs pull up to 3 next-layer weight-conversion tickets (was 1), on top of prologue + chain DMA reorder
# baseline (speedup 1.0000x reference)
; #define GAS __attribute__((address_space(1)))
; #define LAS __attribute__((address_space(3)))
; DI int rfl(int v) { return __builtin_amdgcn_readfirstlane(v); }
; DI int lbid() { int t = blockIdx.x; asm volatile("" : "+s"(t)); return t; }
; DI int ltid() { int t = threadIdx.x; asm volatile("" : "+v"(t)); return t; }
; DI void w_tickets(LAS unsigned char* lds, const Ctx& c, int l, int budget) {
;     const int tid = ltid(), lane = tid & 63, wave = rfl(tid >> 6);
;     LAS float* scr = (LAS float*)(lds + wave * 16384);
;     volatile LAS int* TK = (volatile LAS int*)(lds + MISC_OFF + 208);
;     GAS unsigned* ctr = (GAS unsigned*)((unsigned*)(c.ws + WS_CTL) + CW_WTK + l * 64);
;     float va[32], vb[32]; WItem wa, wb;
;     for (int k = 0; k < budget; ++k) {
;         __syncthreads();
;         if (tid == 0) TK[0] = (int)__hip_atomic_fetch_add(ctr, 1u, __ATOMIC_RELAXED, __HIP_MEMORY_SCOPE_AGENT);
;         __syncthreads();
;         const int t = rfl(TK[0]); if (t >= W_NTK) break;
; __global__ void __launch_bounds__(NTHREADS, 2) mk_fwd(Ctx c_arg) {
;     ...
;                 if (l + 1 < DEPTH && lbid() >= (TH / 256) * (NIN / 256) % G && (TH / 256) * (NIN / 256) % G != 0) w_tickets(lds, c, l + 1, 1);
.LBB0_319:
	v_readlane_b32 s0, v254, 41
	v_readlane_b32 s1, v254, 42
	s_andn2_b64 vcc, exec, s[0:1]
	s_cbranch_vccnz .LBB0_514
	s_abs_i32 s0, s49
	v_cvt_f32_u32_e32 v1, s0
	s_sub_i32 s4, 0, s0
	s_mov_b32 s1, s2
	v_rcp_iflag_f32_e32 v1, v1
	s_nop 0
	v_mul_f32_e32 v1, 0x4f7ffffe, v1
	v_cvt_u32_f32_e32 v1, v1
	s_nop 0
	v_readfirstlane_b32 s5, v1
	s_mul_i32 s4, s4, s5
	s_mul_hi_u32 s4, s5, s4
	s_add_i32 s5, s5, s4
	s_mul_hi_u32 s4, s5, 0x1380
	s_mul_i32 s4, s4, s0
	s_sub_i32 s4, 0x1380, s4
	s_sub_i32 s5, s4, s0
	s_cmp_ge_u32 s4, s0
	s_cselect_b32 s4, s5, s4
	s_sub_i32 s5, s4, s0
	s_cmp_ge_u32 s4, s0
	s_cselect_b32 s4, s5, s4
	s_cmp_lt_i32 s1, s4
	s_cselect_b64 s[0:1], -1, 0
	s_cmp_eq_u32 s4, 0
	s_cselect_b64 s[4:5], -1, 0
	s_or_b64 s[0:1], s[0:1], s[4:5]
	s_and_b64 vcc, exec, s[0:1]
	s_cbranch_vccnz .LBB0_514
	v_writelane_b32 v120, s7, 0
	v_writelane_b32 v120, s42, 1
	v_writelane_b32 v120, s43, 2
	v_writelane_b32 v120, s44, 3
	v_writelane_b32 v120, s45, 4
	v_writelane_b32 v120, s48, 5
	v_writelane_b32 v120, s54, 6
	v_writelane_b32 v120, s55, 7
	v_writelane_b32 v120, s56, 8
	v_writelane_b32 v120, s57, 9
	v_writelane_b32 v120, s58, 10
	v_writelane_b32 v120, s59, 11
	v_writelane_b32 v120, s60, 12
	v_writelane_b32 v120, s61, 13
	v_writelane_b32 v120, s62, 14
	v_writelane_b32 v120, s63, 15
	v_writelane_b32 v120, s68, 16
	v_writelane_b32 v120, s76, 17
	v_writelane_b32 v120, s78, 18
	v_writelane_b32 v120, s81, 19
	v_writelane_b32 v120, s82, 20
	v_writelane_b32 v120, s83, 21
	v_writelane_b32 v120, s87, 22
	s_mov_b32 s4, 0
	v_writelane_b32 v120, s4, 23
.Lwta_head:
	v_mov_b32_e32 v1, v0
	s_add_i32 s5, s68, 0x27fd0
	v_readfirstlane_b32 s4, v1
	v_cmp_eq_u32_e32 vcc, 0, v1
	s_waitcnt vmcnt(0)
	s_barrier
	s_and_saveexec_b64 s[0:1], vcc
	s_cbranch_execz .LBB0_325
	s_mov_b64 s[30:31], exec
	v_mbcnt_lo_u32_b32 v2, s30, 0
	v_mbcnt_hi_u32_b32 v2, s31, v2
	v_cmp_eq_u32_e32 vcc, 0, v2
	s_and_saveexec_b64 s[16:17], vcc
	s_cbranch_execz .LBB0_324
	v_readlane_b32 s6, v254, 44
	v_readlane_b32 s7, v254, 45
	s_lshl_b64 s[6:7], s[6:7], 2
	s_add_u32 s6, s58, s6
	s_addc_u32 s7, s59, s7
	s_bcnt1_i32_b64 s8, s[30:31]
	v_mov_b32_e32 v3, s8
	v_mov_b32_e32 v5, 0x28000
	global_atomic_add v3, v5, v3, s[6:7] sc0

; DI int rfl(int v) { return __builtin_amdgcn_readfirstlane(v); }
; DI void w_tickets(LAS unsigned char* lds, const Ctx& c, int l, int budget) {
;     ...
;     for (int k = 0; k < budget; ++k) {
;         __syncthreads();
;         if (tid == 0) TK[0] = (int)__hip_atomic_fetch_add(ctr, 1u, __ATOMIC_RELAXED, __HIP_MEMORY_SCOPE_AGENT);
;         __syncthreads();
;         const int t = rfl(TK[0]); if (t >= W_NTK) break;
;         const int i0 = 32 * t + wave, i1 = i0 + 8, i2 = i0 + 16, i3 = i0 + 24;
;         if (i0 < W_NITEMS) { wa = w_decode(c, l, i0); w_load(wa, lane, va); }
;         if (i1 < W_NITEMS) { wb = w_decode(c, l, i1); w_load(wb, lane, vb); }
;         if (i0 < W_NITEMS) w_store(wa, lane, va, scr);
;         if (i2 < W_NITEMS) { wa = w_decode(c, l, i2); w_load(wa, lane, va); }
;         if (i1 < W_NITEMS) w_store(wb, lane, vb, scr);
;         if (i3 < W_NITEMS) { wb = w_decode(c, l, i3); w_load(wb, lane, vb); }
;         if (i2 < W_NITEMS) w_store(wa, lane, va, scr);
;         if (i3 < W_NITEMS) w_store(wb, lane, vb, scr);
;     }
.Lwta_next:
	v_readlane_b32 s4, v120, 23
	s_add_u32 s4, s4, 1
	s_cmp_ge_u32 s4, 3
	s_cbranch_scc1 .LBB0_514
	v_writelane_b32 v120, s4, 23
	v_readlane_b32 s7, v120, 0
	v_readlane_b32 s42, v120, 1
	v_readlane_b32 s43, v120, 2
	v_readlane_b32 s44, v120, 3
	v_readlane_b32 s45, v120, 4
	v_readlane_b32 s48, v120, 5
	v_readlane_b32 s54, v120, 6
	v_readlane_b32 s55, v120, 7
	v_readlane_b32 s56, v120, 8
	v_readlane_b32 s57, v120, 9
	v_readlane_b32 s58, v120, 10
	v_readlane_b32 s59, v120, 11
	v_readlane_b32 s60, v120, 12
	v_readlane_b32 s61, v120, 13
	v_readlane_b32 s62, v120, 14
	v_readlane_b32 s63, v120, 15
	v_readlane_b32 s68, v120, 16
	v_readlane_b32 s76, v120, 17
	v_readlane_b32 s78, v120, 18
	v_readlane_b32 s81, v120, 19
	v_readlane_b32 s82, v120, 20
	v_readlane_b32 s83, v120, 21
	v_readlane_b32 s87, v120, 22
	s_branch .Lwta_head
